# longconv: bid rotated so that an XCD owns 32 consecutive channels (a contiguous 64-byte piece of each output line) per round
# speedup vs baseline: 1.0058x; 1.0058x over previous
; __device__ __forceinline__ void phase_longconv(const Params& P, unsigned char* smraw, int bid, int nb) {
;     ...
;     const int tid = threadIdx.x, lane = tid & 63, wave = tid >> 6, r = lane & 31, h = lane >> 5;
;     {
;         bfr* Zs = (bfr*)smraw;
;         bfr* Cs = Zs + 129 * HZ_STR;
;         float* Red = (float*)smraw;
;         const int bh = wave & 1, kh = (wave >> 1) & 1, ah = wave >> 2;
;         const int lw = bh + 2 * ah + 4 * kh;
;         for (int c = bid; c < 512; c += nb) {
;             __syncthreads();
;             for (int e = tid; e < 128 * 32; e += NTHR) {
;                 const int row = e >> 5, d4 = (e & 31) * 4;
;                 const float4 v = *(const float4*)(Z + (size_t)c * NT + NCTX + row * 128 + d4);
;                 uint2 pk; pk.x = pack2(v.x, v.y); pk.y = pack2(v.z, v.w);
;                 *(uint2*)&Zs[row * HZ_STR + d4] = pk;
;             }
;             if (tid < HZ_STR / 2) ((unsigned*)&Zs[128 * HZ_STR])[tid] = 0u;
;             f32x16 acc[2][2];
; #pragma unroll
;             for (int i = 0; i < 2; ++i)
; #pragma unroll
;                 for (int j = 0; j < 2; ++j)
; #pragma unroll
;                     for (int q = 0; q < 16; ++q) acc[i][j][q] = 0.f;
;             const float* hf = HF + (size_t)c * 32768 + LSEQ;
;             float w0[3], w1[3], w2[3];
.LBB0_759:
	s_cmp_lt_i32 s6, 5
	s_cselect_b64 s[0:1], -1, 0
	s_cmp_gt_i32 s7, 4
	s_cselect_b64 s[2:3], -1, 0
	s_and_b64 s[0:1], s[0:1], s[2:3]
	s_andn2_b64 vcc, exec, s[0:1]
	s_cbranch_vccnz .LBB0_973
	s_cmpk_gt_i32 s44, 0x1ff
	s_cbranch_scc1 .LBB0_919
	s_add_u32 s58, s42, 0xd1f8000
	s_addc_u32 s59, s43, 0
	v_lshrrev_b32_e32 v3, 2, v0
	s_add_u32 s60, s42, 0x3d5a2400
	v_bfe_u32 v4, v0, 7, 1
	s_movk_i32 s0, 0x44
	v_and_b32_e32 v3, 8, v3
	s_addc_u32 s61, s43, 0
	v_cmp_gt_u32_e64 s[6:7], s0, v0
	v_lshlrev_b32_e32 v5, 1, v3
	v_lshlrev_b32_e32 v7, 7, v4
	s_movk_i32 s0, 0x254
	s_add_u32 s56, s42, 0xf278000
	v_add3_u32 v182, 0, v5, v7
	v_lshrrev_b32_e32 v7, 4, v0
	v_cmp_gt_u32_e64 s[10:11], s0, v0
	s_movk_i32 s0, 0x204
	s_addc_u32 s57, s43, 0
	s_add_i32 s50, 0, 0x20010
	v_and_b32_e32 v7, 28, v7
	v_cmp_gt_u32_e64 s[12:13], s0, v0
	s_movk_i32 s0, 0x203
	v_add_u32_e32 v185, s50, v7
	v_cmp_gt_u32_e64 s[14:15], s0, v0
	v_or_b32_e32 v7, 0x400, v0
	s_movk_i32 s0, 0x454
	v_cmp_gt_u32_e64 s[16:17], s0, v7
	s_movk_i32 s0, 0x404
	v_lshlrev_b32_e32 v186, 1, v0
	v_cmp_gt_u32_e64 s[18:19], s0, v7
	s_movk_i32 s0, 0x403
	v_cmp_gt_u32_e64 s[20:21], s0, v7
	v_add_u32_e32 v8, -8, v186
	s_movk_i32 s0, 0x8a0
	v_cmp_gt_u32_e64 s[22:23], s0, v8
	v_add_u32_e32 v8, -6, v186
	v_cmp_gt_u32_e64 s[24:25], s0, v8
	v_add_u32_e32 v8, -4, v186
	v_lshlrev_b32_e32 v187, 1, v7
	v_cmp_gt_u32_e64 s[26:27], s0, v8
	v_add_u32_e32 v8, -2, v186
	v_cmp_gt_u32_e64 s[28:29], s0, v8
	v_add_u32_e32 v8, -6, v187
	s_mov_b64 s[70:71], s[42:43]
	s_mov_b64 s[68:69], s[40:41]
	v_cmp_gt_u32_e64 s[40:41], s0, v8
	v_add_u32_e32 v8, -4, v187
	s_movk_i32 s1, 0x253
	v_cmp_gt_u32_e64 s[42:43], s0, v8
	v_add_u32_e32 v8, -2, v187
	v_cmp_ne_u32_e64 s[30:31], s1, v0
	s_movk_i32 s1, 0x252
	s_mov_b32 s96, s44
	v_readlane_b32 s66, v253, 10
	s_cmpk_lg_u32 s66, 0x100
	s_mov_b32 s66, s44
	s_cbranch_scc1 .Llc_xcd
	s_and_b32 s66, s44, 7
	s_lshl_b32 s66, s66, 5
	s_lshr_b32 s97, s44, 3
	s_or_b32 s66, s66, s97
.Llc_xcd:
	v_cmp_gt_u32_e64 s[44:45], s0, v8
	s_movk_i32 s0, 0x450
	v_lshrrev_b32_e32 v1, 8, v0
	v_lshl_or_b32 v184, v4, 6, v3
	v_lshlrev_b32_e32 v5, 2, v202
	v_cmp_gt_u32_e64 s[34:35], s1, v0
	s_movk_i32 s1, 0x251
	v_cmp_gt_u32_e64 s[46:47], s0, v7
	v_lshlrev_b32_e32 v4, 16, v4
	v_lshlrev_b32_e32 v7, 8, v0
	v_lshlrev_b32_e32 v2, 2, v0
	v_lshlrev_b32_e32 v172, 6, v1
	v_mov_b32_e32 v3, 0
	v_cmp_gt_u32_e64 s[36:37], s1, v0
	s_movk_i32 s1, 0x250
	v_lshlrev_b32_e32 v1, 15, v1
	v_and_b32_e32 v7, 0x4000, v7
	v_add3_u32 v4, 0, v5, v4
	v_and_b32_e32 v6, 31, v0
	v_cmp_gt_u32_e64 s[38:39], s1, v0
	v_add3_u32 v203, v4, v1, v7
	v_lshl_add_u64 v[4:5], s[70:71], 0, v[2:3]
	s_mov_b64 s[0:1], 0x40662400
	v_add_u32_e32 v147, 0, v2
	v_lshl_add_u64 v[162:163], v[4:5], 0, s[0:1]
	v_lshrrev_b32_e32 v2, 5, v0
	v_lshlrev_b32_e32 v4, 3, v6
	s_movk_i32 s0, 0x110
	v_mad_u32_u24 v4, v2, s0, v4
	v_lshlrev_b32_e32 v2, 9, v2
	v_mov_b32_e32 v7, 0x10400
	v_add3_u32 v206, v4, 0, 16
	v_mad_i64_i32 v[4:5], s[0:1], s66, v7, v[2:3]
	v_lshl_or_b32 v4, v6, 4, v4
	v_lshl_add_u64 v[4:5], s[70:71], 0, v[4:5]
	s_mov_b64 s[0:1], 0xd1f8408
	v_lshl_add_u64 v[164:165], v[4:5], 0, s[0:1]
	v_readlane_b32 s0, v253, 10
	v_add_u32_e32 v4, 0x4100, v0
	v_readlane_b32 s1, v253, 11
	v_lshlrev_b32_e32 v2, 2, v4
	s_ashr_i32 s67, s66, 31
	s_mov_b32 s2, s0
	s_ashr_i32 s3, s0, 31
	s_mul_hi_i32 s63, s0, 0x10400
	s_mul_i32 s62, s0, 0x10400
	v_mad_i64_i32 v[166:167], s[0:1], s66, v7, v[2:3]
	v_lshlrev_b32_e32 v2, 11, v4
	v_lshl_add_u64 v[4:5], s[66:67], 1, v[2:3]
	s_mov_b64 s[0:1], 0xf278400
	v_or_b32_e32 v177, v172, v6
	v_and_b32_e32 v181, 0x58, v0
	v_and_b32_e32 v146, 3, v0
	v_sub_u32_e32 v148, 0xffffc806, v186
	v_sub_u32_e32 v150, 0xffffc408, v186
	v_sub_u32_e32 v152, 0xffffc407, v186
	v_sub_u32_e32 v154, 0xffffc406, v186
	v_sub_u32_e32 v156, 0xffffc808, v187
	v_sub_u32_e32 v158, 0xffffc807, v187
	v_sub_u32_e32 v160, 0xffffc806, v187
	v_or_b32_e32 v204, 0x4000, v0
	v_lshl_add_u64 v[168:169], v[4:5], 0, s[0:1]
	s_mov_b32 s0, s2
	v_mov_b32_e32 v2, 0x20000
	v_or_b32_e32 v173, 0xffffff80, v172
	v_add_u32_e32 v174, -15, v172
	v_or_b32_e32 v175, 32, v172
	v_or_b32_e32 v176, 63, v172
	v_or_b32_e32 v178, 32, v177
	v_or_b32_e32 v179, 31, v172
	v_and_b32_e32 v180, 7, v0
	v_or_b32_e32 v183, 0xffffffa0, v172
	v_cmp_eq_u32_e64 s[8:9], 0, v202
	v_ashrrev_i32_e32 v149, 31, v148
	v_ashrrev_i32_e32 v151, 31, v150
	v_ashrrev_i32_e32 v153, 31, v152
	v_ashrrev_i32_e32 v155, 31, v154
	v_ashrrev_i32_e32 v157, 31, v156
	v_ashrrev_i32_e32 v159, 31, v158
	v_ashrrev_i32_e32 v161, 31, v160
	v_or_b32_e32 v188, 0x80, v181
	v_or_b32_e32 v189, 0x100, v181
	v_or_b32_e32 v190, 0x180, v181
	v_or_b32_e32 v191, 0x200, v181
	v_or_b32_e32 v192, 0x280, v181
	v_or_b32_e32 v193, 0x300, v181
	v_or_b32_e32 v194, 0x380, v181
	v_or_b32_e32 v195, 0x400, v181
	v_or_b32_e32 v196, 0x480, v181
	v_or_b32_e32 v197, 0x500, v181
	v_or_b32_e32 v198, 0x580, v181
	v_or_b32_e32 v199, 0x600, v181
	v_or_b32_e32 v200, 0x680, v181
	v_or_b32_e32 v201, 0x700, v181
	v_mov_b32_e32 v145, v146
	v_or_b32_e32 v1, 0x200, v0
	v_or_b32_e32 v205, 0xfffffe00, v0
	v_writelane_b32 v253, s0, 10
	s_lshl_b64 s[64:65], s[2:3], 1
	v_lshl_or_b32 v207, v0, 3, v2
	v_lshrrev_b32_e32 v208, 8, v204
	v_lshrrev_b32_e32 v209, 6, v204
	v_lshrrev_b32_e32 v210, 1, v204
	v_lshrrev_b32_e32 v211, 7, v204
	s_movk_i32 s51, 0x7fff
	s_add_i32 s70, 0, 0x20020
	v_mov_b32_e32 v212, 0x4400
	v_mov_b32_e32 v213, 0x820
	s_mov_b32 s74, s96
	v_writelane_b32 v253, s1, 11
	s_branch .LBB0_763
